# baseline (speedup 1.0000x reference)
.LBB0_17:
	v_lshlrev_b32_e32 v3, 3, v0
	v_and_b32_e32 v14, 0x1f8, v3
	s_waitcnt vmcnt(0)
	v_ashrrev_i32_e32 v3, 31, v2
	v_lshlrev_b64 v[2:3], 11, v[2:3]
	v_lshl_add_u64 v[2:3], s[50:51], 0, v[2:3]
	v_lshlrev_b32_e32 v10, 2, v14
	v_mov_b32_e32 v11, 0
	v_lshl_add_u64 v[12:13], v[2:3], 0, v[10:11]
	global_load_dwordx4 v[2:5], v[12:13], off offset:16
	global_load_dwordx4 v[6:9], v[12:13], off
	v_lshlrev_b32_e32 v10, 10, v1
	v_lshl_add_u64 v[12:13], s[66:67], 0, v[10:11]
	v_lshlrev_b32_e32 v10, 1, v14
	s_waitcnt vmcnt(1)
	v_cvt_pk_f16_f32 v5, v4, v5
	v_cvt_pk_f16_f32 v4, v2, v3
	s_waitcnt vmcnt(0)
	v_cvt_pk_f16_f32 v3, v8, v9
	v_cvt_pk_f16_f32 v2, v6, v7
	v_lshl_add_u64 v[6:7], v[12:13], 0, v[10:11]
	global_store_dwordx4 v[6:7], v[2:5], off

.LBB0_20:
	s_andn2_b64 vcc, exec, s[20:21]
	s_cbranch_vccnz .LBB0_24
	v_lshl_or_b32 v1, s2, 8, v0
	v_add_u32_e32 v1, 0xffd00000, v1
	s_mov_b32 s0, 0x30000
	v_cmp_gt_u32_e32 vcc, s0, v1
	s_and_saveexec_b64 s[0:1], vcc
	s_cbranch_execz .LBB0_23
	v_lshrrev_b32_e32 v1, 6, v1
	v_lshlrev_b32_e32 v2, 3, v0
	s_movk_i32 s3, 0x600
	v_and_b32_e32 v14, 0x1f8, v2
	v_mul_lo_u32 v10, v1, s3
	v_mov_b32_e32 v11, 0
	s_waitcnt lgkmcnt(0)
	v_lshl_add_u64 v[2:3], v[10:11], 2, s[36:37]
	v_lshlrev_b32_e32 v10, 2, v14
	v_lshl_add_u64 v[12:13], v[2:3], 0, v[10:11]
	global_load_dwordx4 v[2:5], v[12:13], off offset:16
	global_load_dwordx4 v[6:9], v[12:13], off
	v_lshlrev_b32_e32 v10, 10, v1
	v_lshl_add_u64 v[12:13], s[64:65], 0, v[10:11]
	v_lshlrev_b32_e32 v10, 1, v14
	s_waitcnt vmcnt(1)
	v_cvt_pk_f16_f32 v5, v4, v5
	v_cvt_pk_f16_f32 v4, v2, v3
	s_waitcnt vmcnt(0)
	v_cvt_pk_f16_f32 v3, v8, v9
	v_cvt_pk_f16_f32 v2, v6, v7
	v_lshl_add_u64 v[6:7], v[12:13], 0, v[10:11]
	global_store_dwordx4 v[6:7], v[2:5], off

.LBB0_25:
	s_andn2_b64 vcc, exec, s[20:21]
	s_cbranch_vccnz .LBB0_29
	s_add_i32 s0, s2, 0xffffd200
	s_mov_b32 s1, 0
	s_lshl_b64 s[0:1], s[0:1], 8
	v_or_b32_e32 v2, s0, v0
	v_mov_b32_e32 v3, s1
	s_mov_b64 s[0:1], 0x20000
	v_cmp_gt_u64_e32 vcc, s[0:1], v[2:3]
	s_and_saveexec_b64 s[0:1], vcc
	s_cbranch_execz .LBB0_28
	v_lshrrev_b64 v[10:11], 7, v[2:3]
	v_lshlrev_b32_e32 v1, 3, v0
	v_and_b32_e32 v1, 0x3f8, v1
	v_lshlrev_b64 v[2:3], 13, v[10:11]
	s_waitcnt lgkmcnt(0)
	v_lshl_add_u64 v[2:3], s[44:45], 0, v[2:3]
	v_lshlrev_b32_e32 v12, 2, v1
	v_mov_b32_e32 v13, 0
	v_lshl_add_u64 v[14:15], v[2:3], 0, v[12:13]
	global_load_dwordx4 v[2:5], v[14:15], off
	global_load_dwordx4 v[6:9], v[14:15], off offset:16
	v_lshlrev_b64 v[10:11], 12, v[10:11]
	v_mov_b32_e32 v16, 1
	v_lshl_add_u64 v[10:11], s[14:15], 0, v[10:11]
	v_lshlrev_b32_e32 v12, 1, v1
	s_movk_i32 s3, 0x7fff
	v_lshl_add_u64 v[14:15], v[10:11], 0, v[12:13]
	s_mov_b32 s4, 0x7060302
	s_waitcnt vmcnt(1)
	v_and_b32_sdwa v1, v3, v16 dst_sel:DWORD dst_unused:UNUSED_PAD src0_sel:WORD_1 src1_sel:DWORD
	v_and_b32_sdwa v10, v2, v16 dst_sel:DWORD dst_unused:UNUSED_PAD src0_sel:WORD_1 src1_sel:DWORD
	v_and_b32_sdwa v11, v5, v16 dst_sel:DWORD dst_unused:UNUSED_PAD src0_sel:WORD_1 src1_sel:DWORD
	v_and_b32_sdwa v12, v4, v16 dst_sel:DWORD dst_unused:UNUSED_PAD src0_sel:WORD_1 src1_sel:DWORD
	s_waitcnt vmcnt(0)
	v_and_b32_sdwa v13, v7, v16 dst_sel:DWORD dst_unused:UNUSED_PAD src0_sel:WORD_1 src1_sel:DWORD
	v_and_b32_sdwa v17, v6, v16 dst_sel:DWORD dst_unused:UNUSED_PAD src0_sel:WORD_1 src1_sel:DWORD
	v_and_b32_sdwa v18, v9, v16 dst_sel:DWORD dst_unused:UNUSED_PAD src0_sel:WORD_1 src1_sel:DWORD
	v_and_b32_sdwa v16, v8, v16 dst_sel:DWORD dst_unused:UNUSED_PAD src0_sel:WORD_1 src1_sel:DWORD
	v_add3_u32 v1, v3, v1, s3
	v_add3_u32 v10, v2, v10, s3
	v_add3_u32 v11, v5, v11, s3
	v_add3_u32 v24, v4, v12, s3
	v_add3_u32 v12, v7, v13, s3
	v_add3_u32 v25, v6, v17, s3
	v_add3_u32 v13, v9, v18, s3
	v_add3_u32 v26, v8, v16, s3
	v_and_b32_e32 v17, 0xffff0000, v1
	v_and_b32_e32 v16, 0xffff0000, v10
	v_and_b32_e32 v19, 0xffff0000, v11
	v_and_b32_e32 v18, 0xffff0000, v24
	v_and_b32_e32 v21, 0xffff0000, v12
	v_and_b32_e32 v20, 0xffff0000, v25
	v_and_b32_e32 v23, 0xffff0000, v13
	v_and_b32_e32 v22, 0xffff0000, v26
	v_pk_add_f32 v[2:3], v[2:3], v[16:17] neg_lo:[0,1] neg_hi:[0,1]
	v_pk_add_f32 v[4:5], v[4:5], v[18:19] neg_lo:[0,1] neg_hi:[0,1]
	v_pk_add_f32 v[6:7], v[6:7], v[20:21] neg_lo:[0,1] neg_hi:[0,1]
	v_pk_add_f32 v[8:9], v[8:9], v[22:23] neg_lo:[0,1] neg_hi:[0,1]
	v_perm_b32 v10, v1, v10, s4
	v_bfe_u32 v1, v9, 16, 1
	v_bfe_u32 v16, v8, 16, 1
	v_bfe_u32 v17, v7, 16, 1
	v_bfe_u32 v18, v6, 16, 1
	v_bfe_u32 v19, v5, 16, 1
	v_bfe_u32 v20, v4, 16, 1
	v_bfe_u32 v21, v3, 16, 1
	v_bfe_u32 v22, v2, 16, 1
	v_perm_b32 v13, v13, v26, s4
	v_perm_b32 v12, v12, v25, s4
	v_perm_b32 v11, v11, v24, s4
	v_add3_u32 v2, v2, v22, s3
	v_add3_u32 v21, v3, v21, s3
	v_add3_u32 v3, v4, v20, s3
	v_add3_u32 v19, v5, v19, s3
	v_add3_u32 v4, v6, v18, s3
	v_add3_u32 v6, v7, v17, s3
	v_add3_u32 v5, v8, v16, s3
	v_add3_u32 v1, v9, v1, s3
	v_perm_b32 v5, v1, v5, s4
	v_perm_b32 v4, v6, v4, s4
	v_perm_b32 v3, v19, v3, s4
	v_perm_b32 v2, v21, v2, s4
	global_store_dwordx4 v[14:15], v[10:13], off
	global_store_dwordx4 v[14:15], v[2:5], off offset:2048

.LBB0_30:
	s_andn2_b64 vcc, exec, s[20:21]
	s_cbranch_vccnz .LBB0_34
	v_lshl_or_b32 v1, s2, 8, v0
	v_add_u32_e32 v2, 0xffd40000, v1
	s_mov_b32 s0, 0x20000
	v_cmp_gt_u32_e32 vcc, s0, v2
	s_and_saveexec_b64 s[0:1], vcc
	s_cbranch_execz .LBB0_33
	v_lshrrev_b32_e32 v1, 7, v2
	v_and_b32_e32 v3, 15, v0
	s_movk_i32 s3, 0x3f0
	v_and_or_b32 v1, v1, s3, v3
	v_lshlrev_b32_e32 v12, 13, v1
	v_mov_b32_e32 v13, 0
	v_lshlrev_b32_e32 v1, 1, v2
	s_waitcnt lgkmcnt(0)
	v_lshl_add_u64 v[4:5], s[44:45], 0, v[12:13]
	v_and_b32_e32 v12, 0xf80, v1
	v_lshlrev_b32_e32 v1, 1, v0
	v_lshl_add_u64 v[4:5], v[4:5], 0, v[12:13]
	v_and_b32_e32 v12, 0x60, v1
	v_lshl_add_u64 v[8:9], v[4:5], 0, v[12:13]
	s_movk_i32 s3, 0x1000
	s_mov_b64 s[4:5], 0x1000
	v_add_co_u32_e32 v4, vcc, s3, v8
	v_mov_b32_e32 v16, s62
	s_nop 0
	v_addc_co_u32_e32 v5, vcc, 0, v9, vcc
	v_lshl_add_u64 v[8:9], v[8:9], 0, s[4:5]
	global_load_dwordx4 v[4:7], v[4:5], off
	v_mov_b32_e32 v17, s63
	global_load_dwordx4 v[8:11], v[8:9], off offset:16
	v_mov_b32_e32 v3, v13
	v_lshl_add_u64 v[2:3], v[2:3], 4, v[16:17]
	s_waitcnt vmcnt(1)
	v_cvt_pk_f16_f32 v13, v6, v7
	v_cvt_pk_f16_f32 v12, v4, v5
	s_waitcnt vmcnt(0)
	v_cvt_pk_f16_f32 v15, v10, v11
	v_cvt_pk_f16_f32 v14, v8, v9
	global_store_dwordx4 v[2:3], v[12:15], off

.LBB0_42:
	s_andn2_b64 vcc, exec, s[20:21]
	s_cbranch_vccnz .LBB0_46
	v_lshl_or_b32 v1, s2, 8, v0
	v_add_u32_e32 v2, 0xffe40000, v1
	s_mov_b32 s0, 0xc0000
	v_cmp_gt_u32_e32 vcc, s0, v2
	s_and_saveexec_b64 s[0:1], vcc
	s_cbranch_execz .LBB0_45
	v_lshrrev_b32_e32 v1, 6, v2
	v_mul_u32_u24_e32 v3, 0xaaab, v1
	v_lshrrev_b32_e32 v3, 17, v3
	v_mul_lo_u16_e32 v3, 3, v3
	s_mov_b32 s3, 0xaaaaaaab
	v_sub_u16_e32 v1, v1, v3
	v_mul_hi_u32 v3, v2, s3
	v_bfe_u32 v10, v3, 7, 6
	v_lshrrev_b32_e32 v3, 9, v3
	v_lshlrev_b16_e32 v1, 10, v1
	v_and_b32_e32 v3, 0x7f0, v3
	v_add_u32_e32 v1, v3, v1
	v_and_or_b32 v1, v0, 15, v1
	v_lshlrev_b32_e32 v12, 12, v1
	v_mov_b32_e32 v13, 0
	s_waitcnt lgkmcnt(0)
	v_lshl_add_u64 v[4:5], s[42:43], 0, v[12:13]
	v_lshlrev_b32_e32 v6, 7, v10
	v_mov_b32_e32 v7, v13
	s_movk_i32 s4, 0xf000
	v_lshl_add_u64 v[4:5], v[4:5], 0, v[6:7]
	s_mov_b32 s5, -1
	v_lshl_add_u64 v[8:9], s[40:41], 0, v[12:13]
	v_lshl_add_u64 v[4:5], v[4:5], 0, s[4:5]
	v_lshl_add_u64 v[6:7], v[8:9], 0, v[6:7]
	v_cmp_gt_u32_e32 vcc, 32, v10
	v_lshlrev_b32_e32 v1, 1, v0
	v_and_b32_e32 v12, 0x60, v1
	v_cndmask_b32_e32 v5, v5, v7, vcc
	v_cndmask_b32_e32 v4, v4, v6, vcc
	v_lshl_add_u64 v[14:15], v[4:5], 0, v[12:13]
	global_load_dwordx4 v[4:7], v[14:15], off offset:16
	global_load_dwordx4 v[8:11], v[14:15], off
	v_mov_b32_e32 v14, s60
	v_mov_b32_e32 v15, s61
	v_mov_b32_e32 v3, v13
	v_lshl_add_u64 v[2:3], v[2:3], 4, v[14:15]
	s_waitcnt vmcnt(1)
	v_cvt_pk_f16_f32 v7, v6, v7
	v_cvt_pk_f16_f32 v6, v4, v5
	s_waitcnt vmcnt(0)
	v_cvt_pk_f16_f32 v5, v10, v11
	v_cvt_pk_f16_f32 v4, v8, v9
	global_store_dwordx4 v[2:3], v[4:7], off

.LBB0_47:
	s_andn2_b64 vcc, exec, s[20:21]
	s_cbranch_vccnz .LBB0_55
	v_lshl_or_b32 v1, s2, 8, v0
	v_add_u32_e32 v2, 0xfff00000, v1
	s_mov_b32 s0, 0xc0000
	v_cmp_gt_u32_e32 vcc, s0, v2
	s_and_saveexec_b64 s[0:1], vcc
	s_cbranch_execz .LBB0_54
	v_lshrrev_b32_e32 v1, 6, v2
	v_mul_u32_u24_e32 v3, 0xaaab, v1
	v_lshrrev_b32_e32 v3, 17, v3
	v_mul_lo_u16_e32 v3, 3, v3
	s_mov_b32 s3, 0xaaaaaaab
	v_sub_u16_e32 v1, v1, v3
	v_mul_hi_u32 v3, v2, s3
	v_bfe_u32 v4, v3, 7, 6
	v_lshrrev_b32_e32 v3, 9, v3
	v_lshlrev_b16_e32 v1, 10, v1
	v_and_b32_e32 v3, 0x7f0, v3
	v_add_u32_e32 v1, v3, v1
	v_and_or_b32 v1, v0, 15, v1
	v_cmp_lt_u32_e32 vcc, 31, v4
	v_lshlrev_b32_e32 v4, 7, v4
	s_waitcnt lgkmcnt(0)
	s_and_saveexec_b64 s[4:5], vcc
	s_xor_b64 s[4:5], exec, s[4:5]
	v_lshlrev_b32_e32 v6, 12, v1
	v_mov_b32_e32 v7, 0
	v_lshl_add_u64 v[8:9], s[38:39], 0, v[6:7]
	v_mov_b32_e32 v5, v7
	s_movk_i32 s6, 0xf000
	v_lshl_add_u64 v[4:5], v[8:9], 0, v[4:5]
	s_mov_b32 s7, -1
	v_lshl_add_u64 v[6:7], v[4:5], 0, s[6:7]
	s_andn2_saveexec_b64 s[4:5], s[4:5]
	v_mul_u32_u24_e32 v1, 0x600, v1
	v_lshlrev_b32_e32 v6, 2, v1
	v_mov_b32_e32 v7, 0
	v_lshl_add_u64 v[8:9], s[36:37], 0, v[6:7]
	v_mov_b32_e32 v5, v7
	v_lshl_add_u64 v[4:5], v[8:9], 0, v[4:5]
	s_mov_b64 s[6:7], 0x800
	v_lshl_add_u64 v[6:7], v[4:5], 0, s[6:7]
	s_or_b64 exec, exec, s[4:5]
	v_lshlrev_b32_e32 v1, 1, v0
	v_and_b32_e32 v12, 0x60, v1
	v_mov_b32_e32 v13, 0
	v_lshl_add_u64 v[14:15], v[6:7], 0, v[12:13]
	global_load_dwordx4 v[4:7], v[14:15], off offset:16
	global_load_dwordx4 v[8:11], v[14:15], off
	v_mov_b32_e32 v14, s58
	v_mov_b32_e32 v15, s59
	v_mov_b32_e32 v3, v13
	v_lshl_add_u64 v[2:3], v[2:3], 4, v[14:15]
	s_waitcnt vmcnt(1)
	v_cvt_pk_f16_f32 v7, v6, v7
	v_cvt_pk_f16_f32 v6, v4, v5
	s_waitcnt vmcnt(0)
	v_cvt_pk_f16_f32 v5, v10, v11
	v_cvt_pk_f16_f32 v4, v8, v9
	global_store_dwordx4 v[2:3], v[4:7], off

.LBB0_56:
	s_andn2_b64 vcc, exec, s[20:21]
	s_cbranch_vccnz .LBB0_59
	s_ashr_i32 s3, s2, 31
	s_lshl_b64 s[0:1], s[2:3], 8
	v_or_b32_e32 v2, s0, v0
	v_mov_b32_e32 v3, s1
	s_mov_b64 s[0:1], 0x100000
	v_cmp_gt_u64_e32 vcc, s[0:1], v[2:3]
	s_and_saveexec_b64 s[0:1], vcc
	s_cbranch_execz .LBB0_59
	v_lshlrev_b32_e32 v0, 3, v0
	v_and_b32_e32 v12, 0x3f8, v0
	v_lshlrev_b32_e32 v0, 5, v2
	v_and_b32_e32 v8, 0x1fff000, v0
	v_mov_b32_e32 v9, 0
	s_waitcnt lgkmcnt(0)
	v_lshl_add_u64 v[0:1], s[48:49], 0, v[8:9]
	v_lshlrev_b32_e32 v2, 2, v12
	v_mov_b32_e32 v3, v9
	v_lshl_add_u64 v[10:11], v[0:1], 0, v[2:3]
	global_load_dwordx4 v[0:3], v[10:11], off
	global_load_dwordx4 v[4:7], v[10:11], off offset:16
	v_mov_b32_e32 v14, 1
	v_lshl_add_u64 v[10:11], s[10:11], 0, v[8:9]
	v_lshlrev_b32_e32 v8, 1, v12
	s_movk_i32 s0, 0x7fff
	v_lshl_add_u64 v[12:13], v[10:11], 0, v[8:9]
	s_mov_b32 s1, 0x7060302
	s_waitcnt vmcnt(1)
	v_and_b32_sdwa v8, v1, v14 dst_sel:DWORD dst_unused:UNUSED_PAD src0_sel:WORD_1 src1_sel:DWORD
	v_and_b32_sdwa v9, v0, v14 dst_sel:DWORD dst_unused:UNUSED_PAD src0_sel:WORD_1 src1_sel:DWORD
	v_and_b32_sdwa v10, v3, v14 dst_sel:DWORD dst_unused:UNUSED_PAD src0_sel:WORD_1 src1_sel:DWORD
	v_and_b32_sdwa v11, v2, v14 dst_sel:DWORD dst_unused:UNUSED_PAD src0_sel:WORD_1 src1_sel:DWORD
	s_waitcnt vmcnt(0)
	v_and_b32_sdwa v15, v5, v14 dst_sel:DWORD dst_unused:UNUSED_PAD src0_sel:WORD_1 src1_sel:DWORD
	v_and_b32_sdwa v16, v4, v14 dst_sel:DWORD dst_unused:UNUSED_PAD src0_sel:WORD_1 src1_sel:DWORD
	v_and_b32_sdwa v17, v7, v14 dst_sel:DWORD dst_unused:UNUSED_PAD src0_sel:WORD_1 src1_sel:DWORD
	v_and_b32_sdwa v14, v6, v14 dst_sel:DWORD dst_unused:UNUSED_PAD src0_sel:WORD_1 src1_sel:DWORD
	v_add3_u32 v8, v1, v8, s0
	v_add3_u32 v22, v0, v9, s0
	v_add3_u32 v9, v3, v10, s0
	v_add3_u32 v23, v2, v11, s0
	v_add3_u32 v10, v5, v15, s0
	v_add3_u32 v24, v4, v16, s0
	v_add3_u32 v11, v7, v17, s0
	v_add3_u32 v25, v6, v14, s0
	v_and_b32_e32 v15, 0xffff0000, v8
	v_and_b32_e32 v14, 0xffff0000, v22
	v_and_b32_e32 v17, 0xffff0000, v9
	v_and_b32_e32 v16, 0xffff0000, v23
	v_and_b32_e32 v19, 0xffff0000, v10
	v_and_b32_e32 v18, 0xffff0000, v24
	v_and_b32_e32 v21, 0xffff0000, v11
	v_and_b32_e32 v20, 0xffff0000, v25
	v_pk_add_f32 v[0:1], v[0:1], v[14:15] neg_lo:[0,1] neg_hi:[0,1]
	v_pk_add_f32 v[2:3], v[2:3], v[16:17] neg_lo:[0,1] neg_hi:[0,1]
	v_pk_add_f32 v[4:5], v[4:5], v[18:19] neg_lo:[0,1] neg_hi:[0,1]
	v_pk_add_f32 v[6:7], v[6:7], v[20:21] neg_lo:[0,1] neg_hi:[0,1]
	v_bfe_u32 v16, v5, 16, 1
	v_bfe_u32 v14, v7, 16, 1
	v_bfe_u32 v15, v6, 16, 1
	v_bfe_u32 v17, v4, 16, 1
	v_bfe_u32 v18, v3, 16, 1
	v_bfe_u32 v19, v2, 16, 1
	v_bfe_u32 v20, v1, 16, 1
	v_bfe_u32 v21, v0, 16, 1
	v_perm_b32 v11, v11, v25, s1
	v_perm_b32 v10, v10, v24, s1
	v_perm_b32 v9, v9, v23, s1
	v_perm_b32 v8, v8, v22, s1
	v_add3_u32 v0, v0, v21, s0
	v_add3_u32 v20, v1, v20, s0
	v_add3_u32 v1, v2, v19, s0
	v_add3_u32 v18, v3, v18, s0
	v_add3_u32 v2, v4, v17, s0
	v_add3_u32 v4, v5, v16, s0
	v_add3_u32 v3, v6, v15, s0
	v_add3_u32 v5, v7, v14, s0
	v_perm_b32 v3, v5, v3, s1
	v_perm_b32 v2, v4, v2, s1
	v_perm_b32 v1, v18, v1, s1
	v_perm_b32 v0, v20, v0, s1
	global_store_dwordx4 v[12:13], v[8:11], off
	global_store_dwordx4 v[12:13], v[0:3], off offset:2048
